# speedup vs baseline: 1.0172x; 1.0172x over previous
.LBB0_18:
	s_or_b64 exec, exec, s[0:1]
	v_ashrrev_i32_e32 v19, 31, v18
	v_lshlrev_b64 v[24:25], 5, v[18:19]
	v_lshl_add_u64 v[20:21], v[20:21], 0, v[24:25]
	global_load_dwordx4 v[24:27], v[20:21], off offset:16 nt
	global_load_dwordx4 v[28:31], v[20:21], off nt
	v_ashrrev_i32_e32 v11, 7, v14
	v_ashrrev_i32_e32 v19, 7, v18
	s_waitcnt vmcnt(3)
	v_cvt_pk_f16_f32 v7, v6, v7
	v_cvt_pk_f16_f32 v6, v4, v5
	s_waitcnt vmcnt(2)
	v_cvt_pk_f16_f32 v4, v0, v1
	v_add_u32_e32 v0, v11, v23
	v_cvt_pk_f16_f32 v5, v2, v3
	v_add_u32_e32 v2, v19, v22
	v_ashrrev_i32_e32 v1, 31, v0
	v_bfe_u32 v20, v18, 3, 4
	v_ashrrev_i32_e32 v3, 31, v2
	v_mad_u64_u32 v[0:1], s[0:1], v12, v13, v[0:1]
	v_and_b32_e32 v14, 7, v14
	v_mad_u64_u32 v[2:3], s[0:1], v10, v20, v[2:3]
	v_lshlrev_b64 v[0:1], 7, v[0:1]
	v_and_b32_e32 v18, 7, v18
	v_mov_b32_e32 v15, 0
	v_lshlrev_b32_e32 v14, 4, v14
	v_lshlrev_b64 v[2:3], 7, v[2:3]
	v_lshl_add_u64 v[0:1], v[8:9], 0, v[0:1]
	v_lshl_add_u64 v[8:9], v[16:17], 0, v[2:3]
	v_lshl_add_u64 v[0:1], v[0:1], 0, v[14:15]
	v_lshlrev_b32_e32 v14, 4, v18
	global_store_dwordx4 v[0:1], v[4:7], off
	s_waitcnt vmcnt(2)
	v_cvt_pk_f16_f32 v3, v26, v27
	v_cvt_pk_f16_f32 v2, v24, v25
	s_waitcnt vmcnt(1)
	v_cvt_pk_f16_f32 v1, v30, v31
	v_cvt_pk_f16_f32 v0, v28, v29
	v_lshl_add_u64 v[4:5], v[8:9], 0, v[14:15]
	global_store_dwordx4 v[4:5], v[0:3], off
	s_endpgm
	.p2align	8

.LBB1_298:
	v_max_f32_e32 v66, v66, v66
	v_max_f32_e32 v80, 0, v66
	v_exp_f32_e64 v82, -v80
	v_add_f32_e32 v66, v208, v80
	v_xor_b32_e32 v66, 0x80000000, v66
	v_sub_f32_e32 v65, v65, v80
	v_sub_f32_e32 v64, v64, v80
	v_sub_f32_e32 v63, v63, v80
	v_sub_f32_e32 v62, v62, v80
	v_sub_f32_e32 v61, v61, v80
	v_sub_f32_e32 v60, v60, v80
	v_sub_f32_e32 v59, v59, v80
	v_sub_f32_e32 v58, v58, v80
	v_sub_f32_e32 v57, v57, v80
	v_sub_f32_e32 v56, v56, v80
	v_sub_f32_e32 v55, v55, v80
	v_sub_f32_e32 v54, v54, v80
	v_sub_f32_e32 v53, v53, v80
	v_sub_f32_e32 v52, v52, v80
	v_sub_f32_e32 v51, v51, v80
	v_sub_f32_e32 v50, v50, v80
	v_sub_f32_e32 v49, v49, v80
	v_sub_f32_e32 v48, v48, v80
	v_sub_f32_e32 v47, v47, v80
	v_sub_f32_e32 v46, v46, v80
	v_sub_f32_e32 v45, v45, v80
	v_sub_f32_e32 v44, v44, v80
	v_sub_f32_e32 v43, v43, v80
	v_sub_f32_e32 v42, v42, v80
	v_sub_f32_e32 v41, v41, v80
	v_sub_f32_e32 v40, v40, v80
	v_sub_f32_e32 v39, v39, v80
	v_sub_f32_e32 v38, v38, v80
	v_sub_f32_e32 v37, v37, v80
	v_sub_f32_e32 v36, v36, v80
	v_sub_f32_e32 v35, v35, v80
	v_sub_f32_e32 v34, v34, v80
	v_mov_b32_e32 v67, v66
	v_mov_b32_e32 v68, v66
	v_mov_b32_e32 v69, v66
	v_mov_b32_e32 v70, v66
	v_mov_b32_e32 v71, v66
	v_mov_b32_e32 v72, v66
	v_mov_b32_e32 v73, v66
	v_mov_b32_e32 v74, v66
	v_mov_b32_e32 v75, v66
	v_mov_b32_e32 v76, v66
	v_mov_b32_e32 v77, v66
	v_mov_b32_e32 v78, v66
	v_mov_b32_e32 v79, v66
	v_mov_b32_e32 v80, v66
	v_mov_b32_e32 v81, v66
	s_and_saveexec_b64 s[8:9], s[0:1]
	ds_write_b32 v207, v82 offset:49152
	s_or_b64 exec, exec, s[8:9]
	v_mul_f32_e32 v122, v122, v82
	s_branch .LBB1_271
	.p2align	8

_Z11gemm_kernelILi256ELi192ELi4ELi2ELi4ELi2ELi2ELi0EEvPKDF16_S1_iiiPDF16_PfPK15HIP_vector_typeIfLj2EE:
	s_load_dwordx8 s[4:11], s[0:1], 0x0
	s_load_dwordx2 s[12:13], s[0:1], 0x30
	s_lshr_b32 s18, s2, 3
	v_readfirstlane_b32 s17, v0
	s_lshr_b32 s14, s17, 6
	s_waitcnt lgkmcnt(0)
	s_ashr_i32 s11, s8, 31
	s_lshr_b32 s3, s11, 22
	s_add_i32 s3, s8, s3
	s_ashr_i32 s15, s3, 10
	s_abs_i32 s16, s15
	v_cvt_f32_u32_e32 v1, s16
	s_sub_i32 s21, 0, s16
	s_mul_hi_i32 s19, s9, 0x2aaaaaab
	s_lshr_b32 s20, s19, 31
	v_rcp_iflag_f32_e32 v1, v1
	s_ashr_i32 s19, s19, 6
	s_add_i32 s19, s19, s20
	s_bfe_u32 s20, s2, 0x20001
	v_mul_f32_e32 v1, 0x4f7ffffe, v1
	v_cvt_u32_f32_e32 v1, v1
	s_ashr_i32 s3, s3, 31
	s_mul_i32 s20, s15, s20
	v_mov_b32_e32 v97, 0
	v_readfirstlane_b32 s22, v1
	s_mul_i32 s21, s21, s22
	s_mul_hi_u32 s21, s22, s21
	s_add_i32 s22, s22, s21
	s_mul_hi_u32 s22, s18, s22
	s_mul_i32 s21, s22, s16
	s_sub_i32 s23, s18, s21
	s_add_i32 s24, s22, 1
	s_sub_i32 s25, s23, s16
	s_cmp_ge_u32 s23, s16
	s_cselect_b32 s22, s24, s22
	s_cselect_b32 s23, s25, s23
	s_add_i32 s24, s22, 1
	s_cmp_ge_u32 s23, s16
	s_cselect_b32 s16, s24, s22
	s_xor_b32 s16, s16, s3
	s_sub_i32 s3, s16, s3
	s_mul_i32 s15, s3, s15
	s_sub_i32 s15, s18, s15
	s_add_i32 s15, s15, s20
	s_bitcmp1_b32 s2, 0
	v_bfe_u32 v1, v0, 3, 3
	s_cselect_b32 s2, s19, 0
	v_lshl_or_b32 v1, s14, 3, v1
	s_add_i32 s18, s3, s2
	s_lshl_b32 s19, s15, 8
	v_lshrrev_b32_e32 v2, 1, v1
	s_lshl_b32 s2, s14, 10
	v_xor_b32_e32 v6, v2, v0
	v_add_u32_e32 v2, s19, v1
	s_cmp_lg_u32 0, -1
	s_mul_i32 s15, s18, 0xc0
	v_ashrrev_i32_e32 v3, 31, v2
	s_cselect_b32 s3, 0, 0
	v_lshlrev_b64 v[2:3], 7, v[2:3]
	v_add_u32_e32 v4, s15, v1
	s_add_i32 s22, s2, s3
	v_lshlrev_b32_e32 v1, 4, v6
	s_lshr_b32 s3, s17, 1
	v_lshl_add_u64 v[2:3], s[4:5], 0, v[2:3]
	v_ashrrev_i32_e32 v5, 31, v4
	v_and_b32_e32 v96, 0x70, v1
	s_add_i32 s24, s22, 0x8000
	s_and_b32 s20, s3, 0x7fffffc0
	v_lshlrev_b64 v[4:5], 7, v[4:5]
	v_lshl_add_u64 v[104:105], v[2:3], 0, v[96:97]
	s_bitcmp1_b32 s17, 6
	s_mov_b64 s[4:5], 0x2000
	s_mov_b32 m0, s22
	s_nop 0
	global_load_lds_dwordx4 v[104:105], off
	v_lshl_add_u64 v[4:5], s[6:7], 0, v[4:5]
	s_cselect_b32 s16, 0x60, 0
	v_lshl_add_u64 v[110:111], v[104:105], 0, s[4:5]
	s_mov_b64 s[6:7], 0x4000
	s_add_i32 s3, s22, 0x2000
	s_mov_b32 m0, s3
	s_nop 0
	global_load_lds_dwordx4 v[110:111], off
	v_lshl_add_u64 v[108:109], v[104:105], 0, s[6:7]
	s_mov_b64 s[26:27], 0x6000
	s_add_i32 s3, s22, 0x4000
	s_mov_b32 m0, s3
	s_nop 0
	global_load_lds_dwordx4 v[108:109], off
	v_lshl_add_u64 v[106:107], v[104:105], 0, s[26:27]
	s_add_i32 s3, s22, 0x6000
	s_mov_b32 m0, s3
	s_nop 0
	global_load_lds_dwordx4 v[106:107], off
	v_lshl_add_u64 v[98:99], v[4:5], 0, v[96:97]
	s_mov_b32 m0, s24
	s_nop 0
	global_load_lds_dwordx4 v[98:99], off
	v_lshl_add_u64 v[100:101], v[98:99], 0, s[4:5]
	s_add_i32 s3, s22, 0xa000
	s_mov_b32 m0, s3
	s_nop 0
	global_load_lds_dwordx4 v[100:101], off
	v_lshl_add_u64 v[102:103], v[98:99], 0, s[6:7]
	s_add_i32 s3, s22, 0xc000
	s_mov_b32 m0, s3
	s_nop 0
	global_load_lds_dwordx4 v[102:103], off
	s_mov_b32 s21, 1
	s_mov_b32 s23, 0
	s_cmp_lt_i32 s10, 64
	v_mov_b32_e32 v96, v97
	v_mov_b32_e32 v95, v97
	v_mov_b32_e32 v94, v97
	v_mov_b32_e32 v93, v97
	v_mov_b32_e32 v92, v97
	v_mov_b32_e32 v91, v97
	v_mov_b32_e32 v90, v97
	v_mov_b32_e32 v89, v97
	v_mov_b32_e32 v88, v97
	v_mov_b32_e32 v87, v97
	v_mov_b32_e32 v86, v97
	v_mov_b32_e32 v85, v97
	v_mov_b32_e32 v84, v97
	v_mov_b32_e32 v83, v97
	v_mov_b32_e32 v82, v97
	v_mov_b32_e32 v81, v97
	v_mov_b32_e32 v80, v97
	v_mov_b32_e32 v79, v97
	v_mov_b32_e32 v78, v97
	v_mov_b32_e32 v77, v97
	v_mov_b32_e32 v76, v97
	v_mov_b32_e32 v75, v97
	v_mov_b32_e32 v74, v97
	v_mov_b32_e32 v73, v97
	v_mov_b32_e32 v72, v97
	v_mov_b32_e32 v71, v97
	v_mov_b32_e32 v70, v97
	v_mov_b32_e32 v69, v97
	v_mov_b32_e32 v68, v97
	v_mov_b32_e32 v67, v97
	v_mov_b32_e32 v66, v97
	v_mov_b32_e32 v65, v97
	v_mov_b32_e32 v64, v97
	v_mov_b32_e32 v63, v97
	v_mov_b32_e32 v62, v97
	v_mov_b32_e32 v61, v97
	v_mov_b32_e32 v60, v97
	v_mov_b32_e32 v59, v97
	v_mov_b32_e32 v58, v97
	v_mov_b32_e32 v57, v97
	v_mov_b32_e32 v56, v97
	v_mov_b32_e32 v55, v97
	v_mov_b32_e32 v54, v97
	v_mov_b32_e32 v53, v97
	v_mov_b32_e32 v52, v97
	v_mov_b32_e32 v51, v97
	v_mov_b32_e32 v50, v97
	v_mov_b32_e32 v49, v97
	v_mov_b32_e32 v48, v97
	v_mov_b32_e32 v47, v97
	v_mov_b32_e32 v46, v97
	v_mov_b32_e32 v45, v97
	v_mov_b32_e32 v44, v97
	v_mov_b32_e32 v43, v97
	v_mov_b32_e32 v42, v97
	v_mov_b32_e32 v41, v97
	v_mov_b32_e32 v40, v97
	v_mov_b32_e32 v39, v97
	v_mov_b32_e32 v38, v97
	v_mov_b32_e32 v37, v97
	v_mov_b32_e32 v36, v97
	v_mov_b32_e32 v35, v97
	v_mov_b32_e32 v34, v97
	v_mov_b32_e32 v33, v97
	v_mov_b32_e32 v32, v97
	v_mov_b32_e32 v31, v97
	v_mov_b32_e32 v30, v97
	v_mov_b32_e32 v29, v97
	v_mov_b32_e32 v28, v97
	v_mov_b32_e32 v27, v97
	v_mov_b32_e32 v26, v97
	v_mov_b32_e32 v25, v97
	v_mov_b32_e32 v24, v97
	v_mov_b32_e32 v23, v97
	v_mov_b32_e32 v22, v97
	v_mov_b32_e32 v21, v97
	v_mov_b32_e32 v20, v97
	v_mov_b32_e32 v19, v97
	v_mov_b32_e32 v18, v97
	v_mov_b32_e32 v17, v97
	v_mov_b32_e32 v16, v97
	v_mov_b32_e32 v15, v97
	v_mov_b32_e32 v14, v97
	v_mov_b32_e32 v13, v97
	v_mov_b32_e32 v12, v97
	v_mov_b32_e32 v11, v97
	v_mov_b32_e32 v10, v97
	v_mov_b32_e32 v9, v97
	v_mov_b32_e32 v8, v97
	v_mov_b32_e32 v7, v97
	v_mov_b32_e32 v6, v97
	v_mov_b32_e32 v5, v97
	v_mov_b32_e32 v4, v97
	v_mov_b32_e32 v3, v97
	v_mov_b32_e32 v2, v97
	v_and_b32_e32 v162, 31, v0
	v_bfe_u32 v1, v0, 5, 1
	s_cbranch_scc1 .LBB2_6
	s_ashr_i32 s3, s10, 31
	s_lshr_b32 s3, s3, 26
	s_add_i32 s3, s10, s3
	v_lshrrev_b32_e32 v2, 1, v0
	s_ashr_i32 s25, s3, 6
	v_bitop3_b32 v2, v1, v2, 7 bitop3:0x78
	s_cmp_lg_u32 0, -1
	v_lshlrev_b32_e32 v120, 4, v2
	v_or_b32_e32 v2, s20, v162
	s_cselect_b32 s3, 0, 0
	v_lshl_add_u32 v121, v2, 7, 0
	v_or_b32_e32 v2, s16, v162
	s_mov_b32 s10, s8
	s_add_i32 s8, s3, s2
	s_ashr_i32 s3, s9, 31
	s_mov_b32 s2, s9
	v_lshl_add_u32 v122, v2, 7, 0
	s_lshl_b64 s[2:3], s[2:3], 7
	v_mov_b32_e32 v2, 0
	s_addk_i32 s8, 0x6000
	v_xor_b32_e32 v123, 32, v120
	v_xor_b32_e32 v124, 64, v120
	v_xor_b32_e32 v125, 0x60, v120
	s_lshl_b64 s[4:5], s[10:11], 7
	s_mov_b64 s[6:7], s[2:3]
	s_mov_b32 s9, 0
	v_mov_b32_e32 v3, v2
	v_mov_b32_e32 v4, v2
	v_mov_b32_e32 v5, v2
	v_mov_b32_e32 v6, v2
	v_mov_b32_e32 v7, v2
	v_mov_b32_e32 v8, v2
	v_mov_b32_e32 v9, v2
	v_mov_b32_e32 v10, v2
	v_mov_b32_e32 v11, v2
	v_mov_b32_e32 v12, v2
	v_mov_b32_e32 v13, v2
	v_mov_b32_e32 v14, v2
	v_mov_b32_e32 v15, v2
	v_mov_b32_e32 v16, v2
	v_mov_b32_e32 v17, v2
	v_mov_b32_e32 v18, v2
	v_mov_b32_e32 v19, v2
	v_mov_b32_e32 v20, v2
	v_mov_b32_e32 v21, v2
	v_mov_b32_e32 v22, v2
	v_mov_b32_e32 v23, v2
	v_mov_b32_e32 v24, v2
	v_mov_b32_e32 v25, v2
	v_mov_b32_e32 v26, v2
	v_mov_b32_e32 v27, v2
	v_mov_b32_e32 v28, v2
	v_mov_b32_e32 v29, v2
	v_mov_b32_e32 v30, v2
	v_mov_b32_e32 v31, v2
	v_mov_b32_e32 v32, v2
	v_mov_b32_e32 v33, v2
	v_mov_b32_e32 v34, v2
	v_mov_b32_e32 v35, v2
	v_mov_b32_e32 v36, v2
	v_mov_b32_e32 v37, v2
	v_mov_b32_e32 v38, v2
	v_mov_b32_e32 v39, v2
	v_mov_b32_e32 v40, v2
	v_mov_b32_e32 v41, v2
	v_mov_b32_e32 v42, v2
	v_mov_b32_e32 v43, v2
	v_mov_b32_e32 v44, v2
	v_mov_b32_e32 v45, v2
	v_mov_b32_e32 v46, v2
	v_mov_b32_e32 v47, v2
	v_mov_b32_e32 v48, v2
	v_mov_b32_e32 v49, v2
	v_mov_b32_e32 v50, v2
	v_mov_b32_e32 v51, v2
	v_mov_b32_e32 v52, v2
	v_mov_b32_e32 v53, v2
	v_mov_b32_e32 v54, v2
	v_mov_b32_e32 v55, v2
	v_mov_b32_e32 v56, v2
	v_mov_b32_e32 v57, v2
	v_mov_b32_e32 v58, v2
	v_mov_b32_e32 v59, v2
	v_mov_b32_e32 v60, v2
	v_mov_b32_e32 v61, v2
	v_mov_b32_e32 v62, v2
	v_mov_b32_e32 v63, v2
	v_mov_b32_e32 v64, v2
	v_mov_b32_e32 v65, v2
	v_mov_b32_e32 v66, v2
	v_mov_b32_e32 v67, v2
	v_mov_b32_e32 v68, v2
	v_mov_b32_e32 v69, v2
	v_mov_b32_e32 v70, v2
	v_mov_b32_e32 v71, v2
	v_mov_b32_e32 v72, v2
	v_mov_b32_e32 v73, v2
	v_mov_b32_e32 v74, v2
	v_mov_b32_e32 v75, v2
	v_mov_b32_e32 v76, v2
	v_mov_b32_e32 v77, v2
	v_mov_b32_e32 v78, v2
	v_mov_b32_e32 v79, v2
	v_mov_b32_e32 v80, v2
	v_mov_b32_e32 v81, v2
	v_mov_b32_e32 v82, v2
	v_mov_b32_e32 v83, v2
	v_mov_b32_e32 v84, v2
	v_mov_b32_e32 v85, v2
	v_mov_b32_e32 v86, v2
	v_mov_b32_e32 v87, v2
	v_mov_b32_e32 v88, v2
	v_mov_b32_e32 v89, v2
	v_mov_b32_e32 v90, v2
	v_mov_b32_e32 v91, v2
	v_mov_b32_e32 v92, v2
	v_mov_b32_e32 v93, v2
	v_mov_b32_e32 v94, v2
	v_mov_b32_e32 v95, v2
	v_mov_b32_e32 v96, v2
	v_mov_b32_e32 v97, v2
	v_lshl_add_u64 v[168:169], v[104:105], 0, s[4:5]
	v_lshl_add_u64 v[170:171], v[110:111], 0, s[4:5]
	v_lshl_add_u64 v[172:173], v[108:109], 0, s[4:5]
	v_lshl_add_u64 v[174:175], v[106:107], 0, s[4:5]
	v_lshl_add_u64 v[176:177], v[98:99], 0, s[2:3]
	v_lshl_add_u64 v[178:179], v[100:101], 0, s[2:3]
	v_lshl_add_u64 v[180:181], v[102:103], 0, s[2:3]
	s_add_i32 s25, s25, -1
	s_cmp_lt_i32 s9, s25
	s_cbranch_scc0 .Lqkv_last
.Lqkv_loop:
	s_waitcnt vmcnt(0)
	s_barrier
	s_mul_i32 s10, s23, 0xe000
	s_mul_i32 s11, s21, 0xe000
	v_add_u32_e32 v142, s10, v122
	v_add_u32_e32 v143, s10, v121
	s_add_i32 s11, s11, s22
	v_add_u32_e32 v144, v142, v120
	v_add_u32_e32 v145, v143, v120
	ds_read_b128 v[130:133], v145
	ds_read_b128 v[104:107], v144 offset:32768
	ds_read_b128 v[108:111], v144 offset:36864
	ds_read_b128 v[134:137], v145 offset:4096
	ds_read_b128 v[126:129], v144 offset:40960
	s_mov_b32 m0, s11
	s_xor_b32 s23, s23, 1
	global_load_lds_dwordx4 v[168:169], off
	v_lshl_add_u64 v[168:169], v[168:169], 0, s[4:5]
	s_add_i32 m0, s11, 0x2000
	s_xor_b32 s21, s21, 1
	global_load_lds_dwordx4 v[170:171], off
	v_lshl_add_u64 v[170:171], v[170:171], 0, s[4:5]
	v_add_u32_e32 v146, v142, v123
	v_add_u32_e32 v147, v143, v123
	ds_read_b128 v[182:185], v147
	ds_read_b128 v[138:141], v146 offset:32768
	ds_read_b128 v[112:115], v146 offset:36864
	ds_read_b128 v[186:189], v147 offset:4096
	ds_read_b128 v[116:119], v146 offset:40960
	s_waitcnt lgkmcnt(8)
	s_add_i32 m0, s11, 0x4000
	v_mfma_f32_32x32x16_f16 v[82:97], v[104:107], v[130:133], v[82:97]
	global_load_lds_dwordx4 v[172:173], off
	v_lshl_add_u64 v[172:173], v[172:173], 0, s[4:5]
	s_waitcnt lgkmcnt(7)
	v_mfma_f32_32x32x16_f16 v[66:81], v[108:111], v[130:133], v[66:81]
	s_waitcnt lgkmcnt(6)
	s_add_i32 m0, s11, 0x6000
	v_mfma_f32_32x32x16_f16 v[34:49], v[104:107], v[134:137], v[34:49]
	global_load_lds_dwordx4 v[174:175], off
	v_lshl_add_u64 v[174:175], v[174:175], 0, s[4:5]
	v_mfma_f32_32x32x16_f16 v[18:33], v[108:111], v[134:137], v[18:33]
	s_waitcnt lgkmcnt(5)
	v_mfma_f32_32x32x16_f16 v[50:65], v[126:129], v[130:133], v[50:65]
	v_mfma_f32_32x32x16_f16 v[2:17], v[126:129], v[134:137], v[2:17]
	v_add_u32_e32 v144, v142, v124
	v_add_u32_e32 v145, v143, v124
	ds_read_b128 v[130:133], v145
	ds_read_b128 v[104:107], v144 offset:32768
	ds_read_b128 v[108:111], v144 offset:36864
	ds_read_b128 v[134:137], v145 offset:4096
	ds_read_b128 v[126:129], v144 offset:40960
	s_waitcnt lgkmcnt(8)
	s_add_i32 m0, s11, 0x8000
	v_mfma_f32_32x32x16_f16 v[82:97], v[138:141], v[182:185], v[82:97]
	global_load_lds_dwordx4 v[176:177], off
	v_lshl_add_u64 v[176:177], v[176:177], 0, s[2:3]
	s_waitcnt lgkmcnt(7)
	v_mfma_f32_32x32x16_f16 v[66:81], v[112:115], v[182:185], v[66:81]
	s_waitcnt lgkmcnt(6)
	s_add_i32 m0, s11, 0xa000
	v_mfma_f32_32x32x16_f16 v[34:49], v[138:141], v[186:189], v[34:49]
	global_load_lds_dwordx4 v[178:179], off
	v_lshl_add_u64 v[178:179], v[178:179], 0, s[2:3]
	v_mfma_f32_32x32x16_f16 v[18:33], v[112:115], v[186:189], v[18:33]
	s_waitcnt lgkmcnt(5)
	s_add_i32 m0, s11, 0xc000
	v_mfma_f32_32x32x16_f16 v[50:65], v[116:119], v[182:185], v[50:65]
	global_load_lds_dwordx4 v[180:181], off
	v_lshl_add_u64 v[180:181], v[180:181], 0, s[2:3]
	v_mfma_f32_32x32x16_f16 v[2:17], v[116:119], v[186:189], v[2:17]
	v_add_u32_e32 v146, v142, v125
	v_add_u32_e32 v147, v143, v125
	ds_read_b128 v[182:185], v147
	ds_read_b128 v[138:141], v146 offset:32768
	ds_read_b128 v[112:115], v146 offset:36864
	ds_read_b128 v[186:189], v147 offset:4096
	ds_read_b128 v[116:119], v146 offset:40960
	s_waitcnt lgkmcnt(8)
	v_mfma_f32_32x32x16_f16 v[82:97], v[104:107], v[130:133], v[82:97]
	s_waitcnt lgkmcnt(7)
	v_mfma_f32_32x32x16_f16 v[66:81], v[108:111], v[130:133], v[66:81]
	s_waitcnt lgkmcnt(6)
	v_mfma_f32_32x32x16_f16 v[34:49], v[104:107], v[134:137], v[34:49]
	v_mfma_f32_32x32x16_f16 v[18:33], v[108:111], v[134:137], v[18:33]
	s_waitcnt lgkmcnt(5)
	v_mfma_f32_32x32x16_f16 v[50:65], v[126:129], v[130:133], v[50:65]
	v_mfma_f32_32x32x16_f16 v[2:17], v[126:129], v[134:137], v[2:17]
	s_waitcnt lgkmcnt(3)
	v_mfma_f32_32x32x16_f16 v[82:97], v[138:141], v[182:185], v[82:97]
	s_waitcnt lgkmcnt(2)
	v_mfma_f32_32x32x16_f16 v[66:81], v[112:115], v[182:185], v[66:81]
	s_waitcnt lgkmcnt(1)
	v_mfma_f32_32x32x16_f16 v[34:49], v[138:141], v[186:189], v[34:49]
	v_mfma_f32_32x32x16_f16 v[18:33], v[112:115], v[186:189], v[18:33]
	s_waitcnt lgkmcnt(0)
	v_mfma_f32_32x32x16_f16 v[50:65], v[116:119], v[182:185], v[50:65]
	v_mfma_f32_32x32x16_f16 v[2:17], v[116:119], v[186:189], v[2:17]
	s_add_i32 s9, s9, 1
	s_cmp_lt_i32 s9, s25
	s_cbranch_scc1 .Lqkv_loop
.Lqkv_last:
	s_waitcnt vmcnt(0)
	s_barrier
	s_mul_i32 s10, s23, 0xe000
	v_add_u32_e32 v142, s10, v122
	v_add_u32_e32 v143, s10, v121
	v_add_u32_e32 v144, v142, v120
	v_add_u32_e32 v145, v143, v120
	ds_read_b128 v[130:133], v145
	ds_read_b128 v[104:107], v144 offset:32768
	ds_read_b128 v[108:111], v144 offset:36864
	ds_read_b128 v[134:137], v145 offset:4096
	ds_read_b128 v[126:129], v144 offset:40960
	v_add_u32_e32 v146, v142, v123
	v_add_u32_e32 v147, v143, v123
	ds_read_b128 v[182:185], v147
	ds_read_b128 v[138:141], v146 offset:32768
	ds_read_b128 v[112:115], v146 offset:36864
	ds_read_b128 v[186:189], v147 offset:4096
	ds_read_b128 v[116:119], v146 offset:40960
	s_waitcnt lgkmcnt(8)
	v_mfma_f32_32x32x16_f16 v[82:97], v[104:107], v[130:133], v[82:97]
	s_waitcnt lgkmcnt(7)
	v_mfma_f32_32x32x16_f16 v[66:81], v[108:111], v[130:133], v[66:81]
	s_waitcnt lgkmcnt(6)
	v_mfma_f32_32x32x16_f16 v[34:49], v[104:107], v[134:137], v[34:49]
	v_mfma_f32_32x32x16_f16 v[18:33], v[108:111], v[134:137], v[18:33]
	s_waitcnt lgkmcnt(5)
	v_mfma_f32_32x32x16_f16 v[50:65], v[126:129], v[130:133], v[50:65]
	v_mfma_f32_32x32x16_f16 v[2:17], v[126:129], v[134:137], v[2:17]
	v_add_u32_e32 v144, v142, v124
	v_add_u32_e32 v145, v143, v124
	ds_read_b128 v[130:133], v145
	ds_read_b128 v[104:107], v144 offset:32768
	ds_read_b128 v[108:111], v144 offset:36864
	ds_read_b128 v[134:137], v145 offset:4096
	ds_read_b128 v[126:129], v144 offset:40960
	s_waitcnt lgkmcnt(8)
	v_mfma_f32_32x32x16_f16 v[82:97], v[138:141], v[182:185], v[82:97]
	s_waitcnt lgkmcnt(7)
	v_mfma_f32_32x32x16_f16 v[66:81], v[112:115], v[182:185], v[66:81]
	s_waitcnt lgkmcnt(6)
	v_mfma_f32_32x32x16_f16 v[34:49], v[138:141], v[186:189], v[34:49]
	v_mfma_f32_32x32x16_f16 v[18:33], v[112:115], v[186:189], v[18:33]
	s_waitcnt lgkmcnt(5)
	v_mfma_f32_32x32x16_f16 v[50:65], v[116:119], v[182:185], v[50:65]
	v_mfma_f32_32x32x16_f16 v[2:17], v[116:119], v[186:189], v[2:17]
	v_add_u32_e32 v146, v142, v125
	v_add_u32_e32 v147, v143, v125
	ds_read_b128 v[182:185], v147
	ds_read_b128 v[138:141], v146 offset:32768
	ds_read_b128 v[112:115], v146 offset:36864
	ds_read_b128 v[186:189], v147 offset:4096
	ds_read_b128 v[116:119], v146 offset:40960
	s_waitcnt lgkmcnt(8)
	v_mfma_f32_32x32x16_f16 v[82:97], v[104:107], v[130:133], v[82:97]
	s_waitcnt lgkmcnt(7)
	v_mfma_f32_32x32x16_f16 v[66:81], v[108:111], v[130:133], v[66:81]
	s_waitcnt lgkmcnt(6)
	v_mfma_f32_32x32x16_f16 v[34:49], v[104:107], v[134:137], v[34:49]
	v_mfma_f32_32x32x16_f16 v[18:33], v[108:111], v[134:137], v[18:33]
	s_waitcnt lgkmcnt(5)
	v_mfma_f32_32x32x16_f16 v[50:65], v[126:129], v[130:133], v[50:65]
	v_mfma_f32_32x32x16_f16 v[2:17], v[126:129], v[134:137], v[2:17]
	s_waitcnt lgkmcnt(3)
	v_mfma_f32_32x32x16_f16 v[82:97], v[138:141], v[182:185], v[82:97]
	s_waitcnt lgkmcnt(2)
	v_mfma_f32_32x32x16_f16 v[66:81], v[112:115], v[182:185], v[66:81]
	s_waitcnt lgkmcnt(1)
	v_mfma_f32_32x32x16_f16 v[34:49], v[138:141], v[186:189], v[34:49]
	v_mfma_f32_32x32x16_f16 v[18:33], v[112:115], v[186:189], v[18:33]
	s_waitcnt lgkmcnt(0)
	v_mfma_f32_32x32x16_f16 v[50:65], v[116:119], v[182:185], v[50:65]
	v_mfma_f32_32x32x16_f16 v[2:17], v[116:119], v[186:189], v[2:17]

.LBB2_56:
	v_or_b32_e32 v4, 32, v67
	v_cvt_pk_f16_f32 v3, v16, v17
	v_cvt_pk_f16_f32 v2, v14, v15
	v_mul_u32_u24_e32 v0, 0xd0, v4
	ds_write_b64 v1, v[2:3] offset:6832
	v_add3_u32 v0, s11, v0, v76
	v_or_b32_e32 v4, s10, v4
	ds_read_b128 v[0:3], v0
	v_ashrrev_i32_e32 v5, 31, v4
	v_lshlrev_b64 v[4:5], 7, v[4:5]
	v_lshl_add_u64 v[4:5], v[52:53], 0, v[4:5]
	v_mov_b32_e32 v51, 0
	v_or_b32_e32 v10, 32, v77
	v_lshl_add_u64 v[8:9], v[4:5], 0, v[50:51]
	v_mul_u32_u24_e32 v4, 0xd0, v10
	v_add3_u32 v4, s11, v4, v78
	ds_read_b128 v[4:7], v4
	s_waitcnt lgkmcnt(1)
	global_store_dwordx4 v[8:9], v[0:3], off
	v_mov_b32_e32 v57, v51
	v_mov_b32_e32 v61, v51
	v_or_b32_e32 v0, s10, v10
	v_ashrrev_i32_e32 v1, 31, v0
	v_lshlrev_b64 v[0:1], 7, v[0:1]
	v_lshl_add_u64 v[0:1], v[54:55], 0, v[0:1]
	v_lshl_add_u64 v[0:1], v[0:1], 0, v[56:57]
	s_waitcnt lgkmcnt(0)
	global_store_dwordx4 v[0:1], v[4:7], off
	v_or_b32_e32 v10, 32, v81
	v_mov_b32_e32 v65, v51
	v_or_b32_e32 v4, 32, v79
	v_mul_u32_u24_e32 v0, 0xd0, v4
	v_add3_u32 v0, s11, v0, v80
	v_or_b32_e32 v4, s10, v4
	ds_read_b128 v[0:3], v0
	v_ashrrev_i32_e32 v5, 31, v4
	v_lshlrev_b64 v[4:5], 7, v[4:5]
	v_lshl_add_u64 v[4:5], v[58:59], 0, v[4:5]
	v_lshl_add_u64 v[8:9], v[4:5], 0, v[60:61]
	v_mul_u32_u24_e32 v4, 0xd0, v10
	v_add3_u32 v4, s11, v4, v83
	ds_read_b128 v[4:7], v4
	s_waitcnt lgkmcnt(1)
	global_store_dwordx4 v[8:9], v[0:3], off
	v_mov_b32_e32 v71, v51
	v_mov_b32_e32 v75, v51
	v_or_b32_e32 v0, s10, v10
	v_ashrrev_i32_e32 v1, 31, v0
	v_lshlrev_b64 v[0:1], 7, v[0:1]
	v_lshl_add_u64 v[0:1], v[62:63], 0, v[0:1]
	v_lshl_add_u64 v[0:1], v[0:1], 0, v[64:65]
	s_waitcnt lgkmcnt(0)
	global_store_dwordx4 v[0:1], v[4:7], off
	v_or_b32_e32 v10, 32, v86
	s_nop 0
	v_or_b32_e32 v4, 32, v84
	v_mul_u32_u24_e32 v0, 0xd0, v4
	v_add3_u32 v0, s11, v0, v85
	v_or_b32_e32 v4, s10, v4
	ds_read_b128 v[0:3], v0
	v_ashrrev_i32_e32 v5, 31, v4
	v_lshlrev_b64 v[4:5], 7, v[4:5]
	v_lshl_add_u64 v[4:5], v[68:69], 0, v[4:5]
	v_lshl_add_u64 v[8:9], v[4:5], 0, v[70:71]
	v_mul_u32_u24_e32 v4, 0xd0, v10
	v_add3_u32 v4, s11, v4, v87
	ds_read_b128 v[4:7], v4
	s_waitcnt lgkmcnt(1)
	global_store_dwordx4 v[8:9], v[0:3], off
	s_nop 1
	v_or_b32_e32 v0, s10, v10
	v_ashrrev_i32_e32 v1, 31, v0
	v_lshlrev_b64 v[0:1], 7, v[0:1]
	v_lshl_add_u64 v[0:1], v[72:73], 0, v[0:1]
	v_lshl_add_u64 v[0:1], v[0:1], 0, v[74:75]
	s_waitcnt lgkmcnt(0)
	global_store_dwordx4 v[0:1], v[4:7], off
	s_endpgm
	.p2align	8

	.amdhsa_kernel _Z11gemm_kernelILi256ELi192ELi4ELi2ELi4ELi2ELi2ELi0EEvPKDF16_S1_iiiPDF16_PfPK15HIP_vector_typeIfLj2EE
		.amdhsa_group_segment_fixed_size 0
		.amdhsa_private_segment_fixed_size 0
		.amdhsa_kernarg_size 56
		.amdhsa_user_sgpr_count 2
		.amdhsa_user_sgpr_dispatch_ptr 0
		.amdhsa_user_sgpr_queue_ptr 0
		.amdhsa_user_sgpr_kernarg_segment_ptr 1
		.amdhsa_user_sgpr_dispatch_id 0
		.amdhsa_user_sgpr_kernarg_preload_length 0
		.amdhsa_user_sgpr_kernarg_preload_offset 0
		.amdhsa_user_sgpr_private_segment_size 0
		.amdhsa_uses_dynamic_stack 0
		.amdhsa_enable_private_segment 0
		.amdhsa_system_sgpr_workgroup_id_x 1
		.amdhsa_system_sgpr_workgroup_id_y 0
		.amdhsa_system_sgpr_workgroup_id_z 0
		.amdhsa_system_sgpr_workgroup_info 0
		.amdhsa_system_vgpr_workitem_id 0
		.amdhsa_next_free_vgpr 190
		.amdhsa_next_free_sgpr 28
		.amdhsa_accum_offset 192
		.amdhsa_reserve_vcc 1
		.amdhsa_float_round_mode_32 0
		.amdhsa_float_round_mode_16_64 0
		.amdhsa_float_denorm_mode_32 3
		.amdhsa_float_denorm_mode_16_64 3
		.amdhsa_dx10_clamp 1
		.amdhsa_ieee_mode 1
		.amdhsa_fp16_overflow 0
		.amdhsa_tg_split 0
		.amdhsa_exception_fp_ieee_invalid_op 0
		.amdhsa_exception_fp_denorm_src 0
		.amdhsa_exception_fp_ieee_div_zero 0
		.amdhsa_exception_fp_ieee_overflow 0
		.amdhsa_exception_fp_ieee_underflow 0
		.amdhsa_exception_fp_ieee_inexact 0
		.amdhsa_exception_int_div_zero 0
	.end_amdhsa_kernel

.LBB3_9:
	s_or_b32 s1, s19, s17
	v_or_b32_e32 v0, s1, v1
	s_add_i32 s16, s16, s18
	v_lshl_or_b32 v50, v42, 2, s16
	v_ashrrev_i32_e32 v1, 31, v0
	v_mad_i64_i32 v[34:35], s[2:3], v50, s0, 0
	v_lshl_add_u64 v[0:1], v[0:1], 2, s[12:13]
	v_lshl_add_u64 v[34:35], v[34:35], 2, v[0:1]
	s_nop 0
	global_store_dword v[34:35], v18, off nt
	v_or_b32_e32 v18, 1, v50
	v_mad_i64_i32 v[36:37], s[2:3], v18, s0, 0
	v_lshl_add_u64 v[36:37], v[36:37], 2, v[0:1]
	v_or_b32_e32 v18, 2, v50
	global_store_dword v[36:37], v19, off nt
	v_mad_i64_i32 v[18:19], s[2:3], v18, s0, 0
	v_lshl_add_u64 v[18:19], v[18:19], 2, v[0:1]
	global_store_dword v[18:19], v20, off nt
	v_or_b32_e32 v20, 3, v50
	v_mad_i64_i32 v[38:39], s[2:3], v20, s0, 0
	v_lshl_add_u64 v[38:39], v[38:39], 2, v[0:1]
	v_or_b32_e32 v20, 8, v50
	global_store_dword v[38:39], v21, off nt
	v_mad_i64_i32 v[20:21], s[2:3], v20, s0, 0
	v_lshl_add_u64 v[20:21], v[20:21], 2, v[0:1]
	global_store_dword v[20:21], v22, off nt
	v_or_b32_e32 v22, 9, v50
	v_mad_i64_i32 v[40:41], s[2:3], v22, s0, 0
	v_lshl_add_u64 v[40:41], v[40:41], 2, v[0:1]
	v_or_b32_e32 v22, 10, v50
	global_store_dword v[40:41], v23, off nt
	v_mad_i64_i32 v[22:23], s[2:3], v22, s0, 0
	v_lshl_add_u64 v[22:23], v[22:23], 2, v[0:1]
	global_store_dword v[22:23], v24, off nt
	v_or_b32_e32 v24, 11, v50
	v_mad_i64_i32 v[42:43], s[2:3], v24, s0, 0
	v_lshl_add_u64 v[42:43], v[42:43], 2, v[0:1]
	v_or_b32_e32 v24, 16, v50
	global_store_dword v[42:43], v25, off nt
	v_mad_i64_i32 v[24:25], s[2:3], v24, s0, 0
	v_lshl_add_u64 v[24:25], v[24:25], 2, v[0:1]
	global_store_dword v[24:25], v26, off nt
	v_or_b32_e32 v26, 17, v50
	v_mad_i64_i32 v[44:45], s[2:3], v26, s0, 0
	v_lshl_add_u64 v[44:45], v[44:45], 2, v[0:1]
	v_or_b32_e32 v26, 18, v50
	global_store_dword v[44:45], v27, off nt
	v_mad_i64_i32 v[26:27], s[2:3], v26, s0, 0
	v_lshl_add_u64 v[26:27], v[26:27], 2, v[0:1]
	global_store_dword v[26:27], v28, off nt
	v_or_b32_e32 v28, 19, v50
	v_mad_i64_i32 v[46:47], s[2:3], v28, s0, 0
	v_lshl_add_u64 v[46:47], v[46:47], 2, v[0:1]
	v_or_b32_e32 v28, 24, v50
	global_store_dword v[46:47], v29, off nt
	v_mad_i64_i32 v[28:29], s[2:3], v28, s0, 0
	v_lshl_add_u64 v[28:29], v[28:29], 2, v[0:1]
	global_store_dword v[28:29], v30, off nt
	v_or_b32_e32 v30, 25, v50
	v_mad_i64_i32 v[48:49], s[2:3], v30, s0, 0
	v_lshl_add_u64 v[48:49], v[48:49], 2, v[0:1]
	v_or_b32_e32 v30, 26, v50
	global_store_dword v[48:49], v31, off nt
	v_mad_i64_i32 v[30:31], s[2:3], v30, s0, 0
	v_lshl_add_u64 v[30:31], v[30:31], 2, v[0:1]
	global_store_dword v[30:31], v32, off nt
	v_or_b32_e32 v32, 27, v50
	v_mad_i64_i32 v[50:51], s[0:1], v32, s0, 0
	v_lshl_add_u64 v[0:1], v[50:51], 2, v[0:1]
	global_store_dword v[0:1], v33, off nt
	global_store_dword v[34:35], v2, off offset:128 nt
	global_store_dword v[36:37], v3, off offset:128 nt
	global_store_dword v[18:19], v4, off offset:128 nt
	global_store_dword v[38:39], v5, off offset:128 nt
	global_store_dword v[20:21], v6, off offset:128 nt
	global_store_dword v[40:41], v7, off offset:128 nt
	global_store_dword v[22:23], v8, off offset:128 nt
	global_store_dword v[42:43], v9, off offset:128 nt
	global_store_dword v[24:25], v10, off offset:128 nt
	global_store_dword v[44:45], v11, off offset:128 nt
	global_store_dword v[26:27], v12, off offset:128 nt
	global_store_dword v[46:47], v13, off offset:128 nt
	global_store_dword v[28:29], v14, off offset:128 nt
	global_store_dword v[48:49], v15, off offset:128 nt
	global_store_dword v[30:31], v16, off offset:128 nt
	global_store_dword v[0:1], v17, off offset:128 nt
	s_endpgm
	.p2align	8

amdhsa.kernels:
  - .agpr_count:     0
    .args:
      - .actual_access:  read_only
        .address_space:  global
        .offset:         0
        .size:           8
        .value_kind:     global_buffer
      - .actual_access:  read_only
        .address_space:  global
        .offset:         8
        .size:           8
        .value_kind:     global_buffer
      - .actual_access:  read_only
        .address_space:  global
        .offset:         16
        .size:           8
        .value_kind:     global_buffer
      - .actual_access:  read_only
        .address_space:  global
        .offset:         24
        .size:           8
        .value_kind:     global_buffer
      - .actual_access:  read_only
        .address_space:  global
        .offset:         32
        .size:           8
        .value_kind:     global_buffer
      - .actual_access:  read_only
        .address_space:  global
        .offset:         40
        .size:           8
        .value_kind:     global_buffer
      - .actual_access:  write_only
        .address_space:  global
        .offset:         48
        .size:           8
        .value_kind:     global_buffer
      - .actual_access:  write_only
        .address_space:  global
        .offset:         56
        .size:           8
        .value_kind:     global_buffer
      - .actual_access:  read_only
        .address_space:  global
        .offset:         64
        .size:           8
        .value_kind:     global_buffer
      - .actual_access:  write_only
        .address_space:  global
        .offset:         72
        .size:           8
        .value_kind:     global_buffer
      - .actual_access:  write_only
        .address_space:  global
        .offset:         80
        .size:           8
        .value_kind:     global_buffer
      - .offset:         88
        .size:           128
        .value_kind:     by_value
    .group_segment_fixed_size: 0
    .kernarg_segment_align: 8
    .kernarg_segment_size: 216
    .language:       OpenCL C
    .language_version:
      - 2
      - 0
    .max_flat_workgroup_size: 256
    .name:           _Z11prep_kernelPKfS0_S0_S0_S0_PKiPDF16_S3_S3_P15HIP_vector_typeIfLj2EEPi5Freqs
    .private_segment_fixed_size: 0
    .sgpr_count:     22
    .sgpr_spill_count: 0
    .symbol:         _Z11prep_kernelPKfS0_S0_S0_S0_PKiPDF16_S3_S3_P15HIP_vector_typeIfLj2EEPi5Freqs.kd
    .uniform_work_group_size: 1
    .uses_dynamic_stack: false
    .vgpr_count:     32
    .vgpr_spill_count: 0
    .wavefront_size: 64
  - .agpr_count:     0
    .args:
      - .address_space:  global
        .offset:         0
        .size:           8
        .value_kind:     global_buffer
      - .address_space:  global
        .offset:         8
        .size:           8
        .value_kind:     global_buffer
      - .address_space:  global
        .offset:         16
        .size:           8
        .value_kind:     global_buffer
      - .address_space:  global
        .offset:         24
        .size:           8
        .value_kind:     global_buffer
      - .address_space:  global
        .offset:         32
        .size:           8
        .value_kind:     global_buffer
      - .address_space:  global
        .offset:         40
        .size:           8
        .value_kind:     global_buffer
      - .address_space:  global
        .offset:         48
        .size:           8
        .value_kind:     global_buffer
      - .actual_access:  read_only
        .address_space:  global
        .offset:         56
        .size:           8
        .value_kind:     global_buffer
      - .actual_access:  write_only
        .address_space:  global
        .offset:         64
        .size:           8
        .value_kind:     global_buffer
    .group_segment_fixed_size: 0
    .kernarg_segment_align: 8
    .kernarg_segment_size: 72
    .language:       OpenCL C
    .language_version:
      - 2
      - 0
    .max_flat_workgroup_size: 256
    .name:           _ZN3att10attn64_fwdEPKDF16_S1_S1_PDF16_S2_P15HIP_vector_typeIfLj2EEPiPKfS2_
    .private_segment_fixed_size: 0
    .sgpr_count:     78
    .sgpr_spill_count: 0
    .symbol:         _ZN3att10attn64_fwdEPKDF16_S1_S1_PDF16_S2_P15HIP_vector_typeIfLj2EEPiPKfS2_.kd
    .uniform_work_group_size: 1
    .uses_dynamic_stack: false
    .vgpr_count:     240
    .vgpr_spill_count: 0
    .wavefront_size: 64
  - .agpr_count:     0
    .args:
      - .address_space:  global
        .offset:         0
        .size:           8
        .value_kind:     global_buffer
      - .address_space:  global
        .offset:         8
        .size:           8
        .value_kind:     global_buffer
      - .offset:         16
        .size:           4
        .value_kind:     by_value
      - .offset:         20
        .size:           4
        .value_kind:     by_value
      - .offset:         24
        .size:           4
        .value_kind:     by_value
      - .actual_access:  write_only
        .address_space:  global
        .offset:         32
        .size:           8
        .value_kind:     global_buffer
      - .actual_access:  read_only
        .address_space:  global
        .offset:         40
        .size:           8
        .value_kind:     global_buffer
      - .actual_access:  read_only
        .address_space:  global
        .offset:         48
        .size:           8
        .value_kind:     global_buffer
    .group_segment_fixed_size: 0
    .kernarg_segment_align: 8
    .kernarg_segment_size: 56
    .language:       OpenCL C
    .language_version:
      - 2
      - 0
    .max_flat_workgroup_size: 512
    .name:           _Z11gemm_kernelILi256ELi192ELi4ELi2ELi4ELi2ELi2ELi0EEvPKDF16_S1_iiiPDF16_PfPK15HIP_vector_typeIfLj2EE
    .private_segment_fixed_size: 0
    .sgpr_count:     34
    .sgpr_spill_count: 0
    .symbol:         _Z11gemm_kernelILi256ELi192ELi4ELi2ELi4ELi2ELi2ELi0EEvPKDF16_S1_iiiPDF16_PfPK15HIP_vector_typeIfLj2EE.kd
    .uniform_work_group_size: 1
    .uses_dynamic_stack: false
    .vgpr_count:     190
    .vgpr_spill_count: 0
    .wavefront_size: 64
  - .agpr_count:     0
    .args:
      - .address_space:  global
        .offset:         0
        .size:           8
        .value_kind:     global_buffer
      - .address_space:  global
        .offset:         8
        .size:           8
        .value_kind:     global_buffer
      - .offset:         16
        .size:           4
        .value_kind:     by_value
      - .offset:         20
        .size:           4
        .value_kind:     by_value
      - .offset:         24
        .size:           4
        .value_kind:     by_value
      - .actual_access:  read_only
        .address_space:  global
        .offset:         32
        .size:           8
        .value_kind:     global_buffer
      - .actual_access:  write_only
        .address_space:  global
        .offset:         40
        .size:           8
        .value_kind:     global_buffer
      - .actual_access:  read_only
        .address_space:  global
        .offset:         48
        .size:           8
        .value_kind:     global_buffer
    .group_segment_fixed_size: 0
    .kernarg_segment_align: 8
    .kernarg_segment_size: 56
    .language:       OpenCL C
    .language_version:
      - 2
      - 0
    .max_flat_workgroup_size: 512
    .name:           _Z11gemm_kernelILi128ELi128ELi4ELi2ELi8ELi1ELi4ELi1EEvPKDF16_S1_iiiPDF16_PfPK15HIP_vector_typeIfLj2EE
    .private_segment_fixed_size: 0
    .sgpr_count:     31
    .sgpr_spill_count: 0
    .symbol:         _Z11gemm_kernelILi128ELi128ELi4ELi2ELi8ELi1ELi4ELi1EEvPKDF16_S1_iiiPDF16_PfPK15HIP_vector_typeIfLj2EE.kd
    .uniform_work_group_size: 1
    .uses_dynamic_stack: false
    .vgpr_count:     62
    .vgpr_spill_count: 0
    .wavefront_size: 64
